# speedup vs baseline: 1.0058x; 1.0058x over previous
.LBB0_1205:
	s_add_i32 s1, s9, -3
	s_add_i32 s2, s9, -2
	s_add_i32 s3, s9, -1
	v_readlane_b32 s0, v130, s9
	v_readlane_b32 s24, v130, s1
	v_readlane_b32 s2, v130, s2
	v_readlane_b32 s26, v130, s3
	v_lshl_add_u64 v[0:1], s[92:93], 0, v[106:107]
	s_ashr_i32 s1, s0, 31
	s_ashr_i32 s25, s24, 31
	s_ashr_i32 s3, s2, 31
	s_ashr_i32 s27, s26, 31
	v_add_co_u32_e32 v0, vcc, s11, v0
	s_add_u32 s28, s92, s21
	v_mov_b32_e32 v6, 0
	v_addc_co_u32_e32 v1, vcc, 0, v1, vcc
	s_addc_u32 s29, s93, s22
	s_lshl_b64 s[24:25], s[24:25], 11
	v_lshl_add_u64 v[2:3], s[92:93], 0, v[110:111]
	v_lshl_add_u64 v[4:5], s[92:93], 0, v[108:109]
	s_lshl_b64 s[2:3], s[2:3], 11
	s_lshl_b64 s[26:27], s[26:27], 11
	s_lshl_b64 s[0:1], s[0:1], 11
	global_load_dwordx2 v[212:213], v126, s[28:29]
	global_load_dwordx4 v[132:135], v[0:1], off
	global_load_dwordx4 v[136:139], v[2:3], off
	global_load_dwordx4 v[140:143], v[0:1], off offset:2048
	global_load_dwordx4 v[144:147], v[4:5], off
	v_lshl_add_u64 v[0:1], v[112:113], 0, s[24:25]
	v_lshl_add_u64 v[2:3], v[112:113], 0, s[2:3]
	v_lshl_add_u64 v[4:5], v[112:113], 0, s[26:27]
	v_lshl_add_u64 v[8:9], v[112:113], 0, s[0:1]
	global_load_dwordx4 v[92:95], v[0:1], off
	global_load_dwordx4 v[88:91], v[2:3], off
	global_load_dwordx4 v[84:87], v[4:5], off
	global_load_dwordx4 v[80:83], v[8:9], off
	global_load_dwordx4 v[76:79], v[0:1], off offset:1024
	global_load_dwordx4 v[72:75], v[2:3], off offset:1024
	global_load_dwordx4 v[68:71], v[4:5], off offset:1024
	global_load_dwordx4 v[64:67], v[8:9], off offset:1024
	v_lshl_add_u32 v44, v6, 2, v129
	ds_read_b128 v[148:151], v44
	ds_read_b128 v[152:155], v44 offset:1024
	ds_read_b128 v[156:159], v44 offset:8192
	ds_read_b128 v[160:163], v44 offset:9216
	ds_read_b128 v[164:167], v44 offset:2048
	ds_read_b128 v[168:171], v44 offset:3072
	ds_read_b128 v[172:175], v44 offset:10240
	ds_read_b128 v[176:179], v44 offset:11264
	ds_read_b128 v[180:183], v44 offset:4096
	ds_read_b128 v[184:187], v44 offset:5120
	ds_read_b128 v[188:191], v44 offset:12288
	ds_read_b128 v[192:195], v44 offset:13312
	ds_read_b128 v[196:199], v44 offset:6144
	ds_read_b128 v[200:203], v44 offset:7168
	ds_read_b128 v[204:207], v44 offset:14336
	ds_read_b128 v[208:211], v44 offset:15360
	ds_read_b128 v[16:19], v44 offset:16384
	ds_read_b128 v[0:3], v44 offset:17408
	ds_read_b128 v[48:51], v44 offset:24576
	ds_read_b128 v[32:35], v44 offset:25600
	ds_read_b128 v[20:23], v44 offset:18432
	ds_read_b128 v[4:7], v44 offset:19456
	ds_read_b128 v[52:55], v44 offset:26624
	ds_read_b128 v[36:39], v44 offset:27648
	ds_read_b128 v[24:27], v44 offset:20480
	ds_read_b128 v[8:11], v44 offset:21504
	ds_read_b128 v[56:59], v44 offset:28672
	ds_read_b128 v[40:43], v44 offset:29696
	ds_read_b128 v[28:31], v44 offset:22528
	ds_read_b128 v[12:15], v44 offset:23552
	ds_read_b128 v[60:63], v44 offset:30720
	ds_read_b128 v[44:47], v44 offset:31744
	s_add_u32 s4, s4, s6
	s_addc_u32 s5, s5, s7
	s_add_i32 s9, s9, 4
	s_add_u32 s21, s21, s12
	s_addc_u32 s22, s22, s13
	v_lshl_add_u64 v[116:117], s[16:17], 0, v[96:97]
	v_lshl_add_u64 v[118:119], s[16:17], 0, v[98:99]
	v_lshl_add_u64 v[120:121], s[16:17], 0, v[100:101]
	v_lshl_add_u64 v[122:123], s[16:17], 0, v[102:103]
	v_lshl_add_u64 v[124:125], s[16:17], 0, v[104:105]
	v_cmp_lt_u64_e32 vcc, s[4:5], v[114:115]
	s_add_u32 s16, s16, s18
	s_addc_u32 s17, s17, s19
	s_and_b64 s[0:1], exec, vcc
	v_lshl_add_u64 v[108:109], v[108:109], 0, s[14:15]
	v_lshl_add_u64 v[106:107], v[106:107], 0, s[14:15]
	v_lshl_add_u64 v[110:111], v[110:111], 0, s[14:15]
	s_waitcnt vmcnt(11)
	v_mov_b32_e32 v131, v134
	v_mov_b32_e32 v134, v135
	s_nop 0
	v_permlane16_swap_b32_e32 v132, v131
	s_waitcnt vmcnt(10)
	v_mov_b32_e32 v135, v138
	v_permlane16_swap_b32_e32 v133, v134
	s_waitcnt vmcnt(7)
	v_mov_b32_e32 v230, v93
	s_waitcnt vmcnt(2)
	v_mov_b32_e32 v235, v73
	s_waitcnt vmcnt(1)
	v_mov_b32_e32 v236, v69
	s_waitcnt vmcnt(0)
	v_mov_b32_e32 v237, v67
	v_lshlrev_b32_e32 v67, 16, v132
	v_and_b32_e32 v69, 0xffff0000, v132
	v_mov_b32_e32 v138, v139
	v_mov_b32_e32 v139, v142
	v_mov_b32_e32 v142, v143
	v_mov_b32_e32 v143, v146
	v_mov_b32_e32 v146, v147
	v_permlane16_swap_b32_e32 v136, v135
	v_mov_b32_e32 v231, v89
	v_mov_b32_e32 v234, v79
	v_lshlrev_b32_e32 v73, 16, v133
	v_and_b32_e32 v79, 0xffff0000, v133
	v_permlane16_swap_b32_e32 v92, v230
	v_permlane16_swap_b32_e32 v94, v95
	v_permlane16_swap_b32_e32 v72, v235
	v_sub_f32_e32 v133, v69, v212
	v_sub_f32_e32 v132, v67, v212
	v_permlane16_swap_b32_e32 v137, v138
	v_permlane16_swap_b32_e32 v140, v139
	v_permlane16_swap_b32_e32 v141, v142
	v_permlane16_swap_b32_e32 v144, v143
	v_permlane16_swap_b32_e32 v145, v146
	v_lshlrev_b32_e32 v89, 16, v134
	v_and_b32_e32 v93, 0xffff0000, v134
	v_lshlrev_b32_e32 v216, 16, v135
	v_and_b32_e32 v217, 0xffff0000, v135
	v_permlane16_swap_b32_e32 v88, v231
	v_permlane16_swap_b32_e32 v90, v91
	v_permlane16_swap_b32_e32 v68, v236
	v_permlane16_swap_b32_e32 v66, v237
	v_sub_f32_e32 v135, v79, v212
	v_sub_f32_e32 v134, v73, v212
	v_permlane32_swap_b32_e32 v230, v95
	v_mov_b32_e32 v250, v72
	v_pk_mul_f32 v[72:73], v[212:213], v[132:133] op_sel:[1,0]
	v_mov_b32_e32 v232, v87
	v_mov_b32_e32 v233, v83
	v_lshlrev_b32_e32 v83, 16, v131
	v_and_b32_e32 v87, 0xffff0000, v131
	v_lshlrev_b32_e32 v131, 16, v136
	v_and_b32_e32 v147, 0xffff0000, v136
	v_lshlrev_b32_e32 v214, 16, v137
	v_and_b32_e32 v215, 0xffff0000, v137
	v_lshlrev_b32_e32 v218, 16, v138
	v_and_b32_e32 v219, 0xffff0000, v138
	v_lshlrev_b32_e32 v220, 16, v140
	v_and_b32_e32 v221, 0xffff0000, v140
	v_lshlrev_b32_e32 v222, 16, v141
	v_and_b32_e32 v223, 0xffff0000, v141
	v_lshlrev_b32_e32 v224, 16, v139
	v_and_b32_e32 v225, 0xffff0000, v139
	v_lshlrev_b32_e32 v228, 16, v144
	v_and_b32_e32 v229, 0xffff0000, v144
	v_lshlrev_b32_e32 v238, 16, v145
	v_and_b32_e32 v239, 0xffff0000, v145
	v_lshlrev_b32_e32 v240, 16, v143
	v_and_b32_e32 v241, 0xffff0000, v143
	v_permlane32_swap_b32_e32 v231, v91
	v_mov_b32_e32 v251, v68
	v_pk_mul_f32 v[68:69], v[212:213], v[134:135] op_sel:[1,0]
	v_mov_b32_e32 v252, v66
	s_waitcnt lgkmcnt(14)
	v_pk_fma_f32 v[66:67], v[72:73], v[148:149], v[156:157]
	v_cvt_pk_f32_fp8_e32 v[72:73], v230
	v_lshlrev_b32_e32 v226, 16, v142
	v_and_b32_e32 v227, 0xffff0000, v142
	v_lshlrev_b32_e32 v242, 16, v146
	v_and_b32_e32 v243, 0xffff0000, v146
	v_permlane16_swap_b32_e32 v86, v232
	v_permlane16_swap_b32_e32 v82, v233
	v_permlane16_swap_b32_e32 v76, v77
	v_permlane16_swap_b32_e32 v78, v234
	v_sub_f32_e32 v137, v87, v212
	v_sub_f32_e32 v136, v83, v212
	v_sub_f32_e32 v141, v215, v212
	v_sub_f32_e32 v140, v214, v212
	v_sub_f32_e32 v143, v147, v212
	v_sub_f32_e32 v142, v131, v212
	v_sub_f32_e32 v145, v219, v212
	v_sub_f32_e32 v144, v218, v212
	v_sub_f32_e32 v147, v217, v212
	v_sub_f32_e32 v146, v216, v212
	v_sub_f32_e32 v215, v221, v212
	v_sub_f32_e32 v214, v220, v212
	v_sub_f32_e32 v217, v223, v212
	v_sub_f32_e32 v216, v222, v212
	v_sub_f32_e32 v219, v225, v212
	v_sub_f32_e32 v218, v224, v212
	v_sub_f32_e32 v223, v239, v212
	v_sub_f32_e32 v222, v238, v212
	v_sub_f32_e32 v225, v229, v212
	v_sub_f32_e32 v224, v228, v212
	v_sub_f32_e32 v229, v241, v212
	v_sub_f32_e32 v228, v240, v212
	v_mov_b32_e32 v131, v92
	v_pk_fma_f32 v[68:69], v[68:69], v[150:151], v[158:159]
	v_cvt_pk_f32_fp8_sdwa v[148:149], v230 src0_sel:WORD_1
	v_cvt_pk_f32_fp8_e32 v[158:159], v231
	v_permlane16_swap_b32_e32 v84, v85
	v_permlane16_swap_b32_e32 v80, v81
	v_permlane16_swap_b32_e32 v74, v75
	v_permlane16_swap_b32_e32 v70, v71
	v_permlane16_swap_b32_e32 v64, v65
	v_sub_f32_e32 v139, v93, v212
	v_sub_f32_e32 v138, v89, v212
	v_sub_f32_e32 v221, v227, v212
	v_sub_f32_e32 v220, v226, v212
	v_sub_f32_e32 v227, v243, v212
	v_sub_f32_e32 v226, v242, v212
	v_mov_b32_e32 v238, v88
	v_mov_b32_e32 v239, v86
	v_mov_b32_e32 v240, v82
	v_mov_b32_e32 v241, v78
	v_permlane32_swap_b32_e32 v77, v234
	v_pk_mul_f32 v[82:83], v[212:213], v[136:137] op_sel:[1,0]
	v_pk_mul_f32 v[92:93], v[212:213], v[146:147] op_sel:[1,0]
	v_pk_mul_f32 v[132:133], v[212:213], v[144:145] op_sel:[1,0]
	v_pk_mul_f32 v[136:137], v[212:213], v[214:215] op_sel:[1,0]
	v_pk_mul_f32 v[144:145], v[212:213], v[222:223] op_sel:[1,0]
	v_pk_mul_f32 v[146:147], v[212:213], v[228:229] op_sel:[1,0]
	v_permlane32_swap_b32_e32 v131, v94
	v_cvt_pk_f32_fp8_sdwa v[214:215], v231 src0_sel:WORD_1
	v_permlane32_swap_b32_e32 v85, v232
	v_permlane32_swap_b32_e32 v81, v233
	v_permlane32_swap_b32_e32 v235, v75
	v_permlane32_swap_b32_e32 v236, v71
	v_pk_mul_f32 v[78:79], v[212:213], v[138:139] op_sel:[1,0]
	v_pk_mul_f32 v[86:87], v[212:213], v[142:143] op_sel:[1,0]
	v_pk_mul_f32 v[88:89], v[212:213], v[140:141] op_sel:[1,0]
	v_pk_mul_f32 v[134:135], v[212:213], v[216:217] op_sel:[1,0]
	v_pk_mul_f32 v[138:139], v[212:213], v[220:221] op_sel:[1,0]
	v_pk_mul_f32 v[140:141], v[212:213], v[218:219] op_sel:[1,0]
	v_pk_mul_f32 v[142:143], v[212:213], v[224:225] op_sel:[1,0]
	v_pk_mul_f32 v[212:213], v[212:213], v[226:227] op_sel:[1,0]
	v_permlane32_swap_b32_e32 v65, v237
	v_cvt_pk_f32_fp8_e32 v[150:151], v95
	v_cvt_pk_f32_fp8_sdwa v[156:157], v95 src0_sel:WORD_1
	v_permlane32_swap_b32_e32 v238, v90
	v_permlane32_swap_b32_e32 v84, v239
	v_permlane32_swap_b32_e32 v80, v240
	v_permlane32_swap_b32_e32 v76, v241
	v_pk_fma_f32 v[132:133], v[132:133], v[170:171], v[178:179]
	v_pk_fma_f32 v[92:93], v[92:93], v[168:169], v[176:177]
	v_cvt_pk_f32_fp8_e32 v[168:169], v77
	v_cvt_pk_f32_fp8_sdwa v[170:171], v77 src0_sel:WORD_1
	v_cvt_pk_f32_fp8_e32 v[176:177], v234
	v_cvt_pk_f32_fp8_sdwa v[178:179], v234 src0_sel:WORD_1
	v_pk_fma_f32 v[144:145], v[144:145], v[198:199], v[206:207]
	v_pk_fma_f32 v[146:147], v[146:147], v[200:201], v[208:209]
	v_cvt_pk_f32_fp8_e32 v[198:199], v131
	v_cvt_pk_f32_fp8_sdwa v[200:201], v131 src0_sel:WORD_1
	v_pk_fma_f32 v[82:83], v[82:83], v[152:153], v[160:161]
	v_pk_fma_f32 v[78:79], v[78:79], v[154:155], v[162:163]
	v_cvt_pk_f32_fp8_e32 v[152:153], v91
	v_cvt_pk_f32_fp8_sdwa v[154:155], v91 src0_sel:WORD_1
	v_cvt_pk_f32_fp8_e32 v[216:217], v232
	v_pk_fma_f32 v[88:89], v[88:89], v[166:167], v[174:175]
	v_pk_fma_f32 v[86:87], v[86:87], v[164:165], v[172:173]
	v_cvt_pk_f32_fp8_sdwa v[164:165], v232 src0_sel:WORD_1
	v_cvt_pk_f32_fp8_e32 v[174:175], v233
	v_cvt_pk_f32_fp8_sdwa v[218:219], v233 src0_sel:WORD_1
	v_permlane32_swap_b32_e32 v250, v74
	v_cvt_pk_f32_fp8_e32 v[220:221], v235
	v_cvt_pk_f32_fp8_sdwa v[222:223], v235 src0_sel:WORD_1
	v_pk_fma_f32 v[136:137], v[136:137], v[180:181], v[188:189]
	v_pk_fma_f32 v[134:135], v[134:135], v[182:183], v[190:191]
	v_cvt_pk_f32_fp8_e32 v[180:181], v75
	v_cvt_pk_f32_fp8_sdwa v[182:183], v75 src0_sel:WORD_1
	v_cvt_pk_f32_fp8_e32 v[188:189], v236
	v_cvt_pk_f32_fp8_sdwa v[190:191], v236 src0_sel:WORD_1
	v_pk_fma_f32 v[138:139], v[138:139], v[186:187], v[194:195]
	v_cvt_pk_f32_fp8_e32 v[194:195], v237
	v_cvt_pk_f32_fp8_sdwa v[226:227], v237 src0_sel:WORD_1
	v_pk_fma_f32 v[142:143], v[142:143], v[196:197], v[204:205]
	v_pk_fma_f32 v[196:197], v[212:213], v[202:203], v[210:211]
	v_cvt_pk_f32_fp8_e32 v[202:203], v94
	v_cvt_pk_f32_fp8_sdwa v[94:95], v94 src0_sel:WORD_1
	v_cvt_pk_f32_fp8_e32 v[204:205], v238
	v_cvt_pk_f32_fp8_sdwa v[206:207], v238 src0_sel:WORD_1
	v_cvt_pk_f32_fp8_e32 v[212:213], v239
	v_cvt_pk_f32_fp8_sdwa v[228:229], v239 src0_sel:WORD_1
	v_cvt_pk_f32_fp8_e32 v[232:233], v240
	v_cvt_pk_f32_fp8_sdwa v[234:235], v240 src0_sel:WORD_1
	v_cvt_pk_f32_fp8_e32 v[236:237], v76
	v_cvt_pk_f32_fp8_sdwa v[76:77], v76 src0_sel:WORD_1
	v_cvt_pk_f32_fp8_e32 v[238:239], v241
	v_cvt_pk_f32_fp8_sdwa v[240:241], v241 src0_sel:WORD_1
	v_pk_add_f32 v[72:73], v[72:73], 0 op_sel_hi:[1,0]
	v_cvt_pk_f32_fp8_e32 v[160:161], v85
	v_cvt_pk_f32_fp8_sdwa v[162:163], v85 src0_sel:WORD_1
	v_permlane32_swap_b32_e32 v251, v70
	v_cvt_pk_f32_fp8_e32 v[224:225], v71
	v_pk_fma_f32 v[140:141], v[140:141], v[184:185], v[192:193]
	v_cvt_pk_f32_fp8_sdwa v[184:185], v71 src0_sel:WORD_1
	v_cvt_pk_f32_fp8_e32 v[208:209], v90
	v_cvt_pk_f32_fp8_sdwa v[90:91], v90 src0_sel:WORD_1
	v_cvt_pk_f32_fp8_e32 v[210:211], v84
	v_cvt_pk_f32_fp8_sdwa v[84:85], v84 src0_sel:WORD_1
	v_cvt_pk_f32_fp8_e32 v[242:243], v74
	v_cvt_pk_f32_fp8_sdwa v[74:75], v74 src0_sel:WORD_1
	v_cvt_pk_f32_fp8_e32 v[248:249], v250
	v_pk_add_f32 v[72:73], v[72:73], v[158:159]
	v_cvt_pk_f32_fp8_sdwa v[158:159], v250 src0_sel:WORD_1
	v_pk_add_f32 v[148:149], v[148:149], 0 op_sel_hi:[1,0]
	v_cvt_pk_f32_fp8_e32 v[166:167], v81
	v_cvt_pk_f32_fp8_sdwa v[172:173], v81 src0_sel:WORD_1
	v_permlane32_swap_b32_e32 v64, v252
	v_cvt_pk_f32_fp8_e32 v[186:187], v65
	v_cvt_pk_f32_fp8_sdwa v[192:193], v65 src0_sel:WORD_1
	v_cvt_pk_f32_fp8_e32 v[230:231], v80
	v_cvt_pk_f32_fp8_sdwa v[80:81], v80 src0_sel:WORD_1
	v_cvt_pk_f32_fp8_e32 v[244:245], v70
	v_cvt_pk_f32_fp8_sdwa v[70:71], v70 src0_sel:WORD_1
	v_pk_add_f32 v[148:149], v[148:149], v[214:215]
	v_cvt_pk_f32_fp8_e32 v[214:215], v251
	v_cvt_pk_f32_fp8_sdwa v[250:251], v251 src0_sel:WORD_1
	v_cvt_pk_f32_fp8_e32 v[246:247], v64
	v_cvt_pk_f32_fp8_sdwa v[64:65], v64 src0_sel:WORD_1
	v_pk_add_f32 v[150:151], v[150:151], 0 op_sel_hi:[1,0]
	v_pk_add_f32 v[156:157], v[156:157], 0 op_sel_hi:[1,0]
	v_pk_add_f32 v[168:169], v[168:169], 0 op_sel_hi:[1,0]
	v_pk_add_f32 v[170:171], v[170:171], 0 op_sel_hi:[1,0]
	v_pk_add_f32 v[176:177], v[176:177], 0 op_sel_hi:[1,0]
	v_pk_add_f32 v[178:179], v[178:179], 0 op_sel_hi:[1,0]
	v_pk_add_f32 v[198:199], v[198:199], 0 op_sel_hi:[1,0]
	v_pk_add_f32 v[200:201], v[200:201], 0 op_sel_hi:[1,0]
	v_pk_add_f32 v[150:151], v[150:151], v[152:153]
	v_pk_add_f32 v[154:155], v[156:157], v[154:155]
	v_pk_add_f32 v[202:203], v[202:203], 0 op_sel_hi:[1,0]
	v_pk_add_f32 v[94:95], v[94:95], 0 op_sel_hi:[1,0]
	v_pk_add_f32 v[236:237], v[236:237], 0 op_sel_hi:[1,0]
	v_pk_add_f32 v[76:77], v[76:77], 0 op_sel_hi:[1,0]
	v_pk_add_f32 v[240:241], v[240:241], 0 op_sel_hi:[1,0]
	v_pk_add_f32 v[168:169], v[168:169], v[220:221]
	v_pk_add_f32 v[170:171], v[170:171], v[222:223]
	v_pk_add_f32 v[176:177], v[176:177], v[180:181]
	v_pk_add_f32 v[178:179], v[178:179], v[182:183]
	v_pk_add_f32 v[180:181], v[198:199], v[204:205]
	v_pk_add_f32 v[182:183], v[200:201], v[206:207]
	v_pk_add_f32 v[198:199], v[202:203], v[208:209]
	v_pk_add_f32 v[90:91], v[94:95], v[90:91]
	v_pk_add_f32 v[72:73], v[72:73], v[160:161]
	v_pk_add_f32 v[94:95], v[148:149], v[162:163]
	v_pk_add_f32 v[148:149], v[150:151], v[216:217]
	v_pk_add_f32 v[150:151], v[154:155], v[164:165]
	v_pk_add_f32 v[154:155], v[236:237], v[248:249]
	v_pk_add_f32 v[76:77], v[76:77], v[158:159]
	v_pk_add_f32 v[74:75], v[240:241], v[74:75]
	v_pk_add_f32 v[160:161], v[168:169], v[188:189]
	v_pk_add_f32 v[162:163], v[170:171], v[190:191]
	v_pk_add_f32 v[164:165], v[176:177], v[224:225]
	v_pk_add_f32 v[168:169], v[178:179], v[184:185]
	v_pk_add_f32 v[170:171], v[180:181], v[210:211]
	v_pk_add_f32 v[84:85], v[182:183], v[84:85]
	v_pk_mul_f32 v[68:69], v[68:69], s[8:9] op_sel_hi:[1,0]
	v_pk_mul_f32 v[66:67], v[66:67], s[8:9] op_sel_hi:[1,0]
	v_pk_mul_f32 v[78:79], v[78:79], s[8:9] op_sel_hi:[1,0]
	v_pk_mul_f32 v[82:83], v[82:83], s[8:9] op_sel_hi:[1,0]
	v_pk_mul_f32 v[132:133], v[132:133], s[8:9] op_sel_hi:[1,0]
	v_pk_mul_f32 v[92:93], v[92:93], s[8:9] op_sel_hi:[1,0]
	v_pk_mul_f32 v[138:139], v[138:139], s[8:9] op_sel_hi:[1,0]
	v_pk_mul_f32 v[140:141], v[140:141], s[8:9] op_sel_hi:[1,0]
	v_pk_mul_f32 v[196:197], v[196:197], s[8:9] op_sel_hi:[1,0]
	v_pk_mul_f32 v[146:147], v[146:147], s[8:9] op_sel_hi:[1,0]
	v_pk_add_f32 v[176:177], v[198:199], v[212:213]
	v_pk_add_f32 v[72:73], v[72:73], v[166:167]
	v_pk_add_f32 v[94:95], v[94:95], v[172:173]
	v_pk_add_f32 v[148:149], v[148:149], v[174:175]
	v_pk_add_f32 v[150:151], v[150:151], v[218:219]
	v_pk_add_f32 v[154:155], v[154:155], v[214:215]
	v_pk_add_f32 v[76:77], v[76:77], v[250:251]
	v_pk_add_f32 v[70:71], v[74:75], v[70:71]
	v_pk_add_f32 v[74:75], v[160:161], v[186:187]
	v_pk_add_f32 v[160:161], v[162:163], v[192:193]
	v_pk_add_f32 v[162:163], v[164:165], v[194:195]
	v_pk_add_f32 v[164:165], v[168:169], v[226:227]
	v_pk_add_f32 v[166:167], v[170:171], v[230:231]
	v_pk_add_f32 v[80:81], v[84:85], v[80:81]
	v_cvt_pk_f32_fp8_e32 v[152:153], v252
	v_pk_mul_f32 v[86:87], v[86:87], s[8:9] op_sel_hi:[1,0]
	v_pk_mul_f32 v[134:135], v[134:135], s[8:9] op_sel_hi:[1,0]
	v_pk_mul_f32 v[136:137], v[136:137], s[8:9] op_sel_hi:[1,0]
	v_pk_add_f32 v[90:91], v[90:91], v[228:229]
	v_pk_add_f32 v[84:85], v[176:177], v[232:233]
	v_pk_fma_f32 v[72:73], v[72:73], s[10:11], v[82:83] op_sel_hi:[1,0,1]
	v_pk_fma_f32 v[78:79], v[94:95], s[10:11], v[78:79] op_sel_hi:[1,0,1]
	v_pk_fma_f32 v[82:83], v[148:149], s[10:11], v[92:93] op_sel_hi:[1,0,1]
	v_pk_fma_f32 v[92:93], v[150:151], s[10:11], v[132:133] op_sel_hi:[1,0,1]
	v_pk_add_f32 v[94:95], v[154:155], v[246:247]
	v_pk_add_f32 v[64:65], v[76:77], v[64:65]
	v_pk_fma_f32 v[74:75], v[74:75], s[10:11], v[140:141] op_sel_hi:[1,0,1]
	v_pk_fma_f32 v[132:133], v[160:161], s[10:11], v[138:139] op_sel_hi:[1,0,1]
	v_pk_fma_f32 v[138:139], v[162:163], s[10:11], v[146:147] op_sel_hi:[1,0,1]
	v_pk_fma_f32 v[140:141], v[164:165], s[10:11], v[196:197] op_sel_hi:[1,0,1]
	v_pk_fma_f32 v[66:67], v[166:167], s[10:11], v[66:67] op_sel_hi:[1,0,1]
	v_pk_fma_f32 v[68:69], v[80:81], s[10:11], v[68:69] op_sel_hi:[1,0,1]
	v_cvt_pk_f32_fp8_sdwa v[156:157], v252 src0_sel:WORD_1
	v_pk_mul_f32 v[88:89], v[88:89], s[8:9] op_sel_hi:[1,0]
	v_pk_add_f32 v[238:239], v[238:239], 0 op_sel_hi:[1,0]
	v_pk_add_f32 v[90:91], v[90:91], v[234:235]
	v_pk_fma_f32 v[80:81], v[84:85], s[10:11], v[86:87] op_sel_hi:[1,0,1]
	v_pk_fma_f32 v[86:87], v[94:95], s[10:11], v[136:137] op_sel_hi:[1,0,1]
	v_pk_fma_f32 v[64:65], v[64:65], s[10:11], v[134:135] op_sel_hi:[1,0,1]
	v_add_f32_e32 v131, v140, v141
	v_add_f32_e32 v134, v138, v139
	v_add_f32_e32 v135, v68, v69
	v_add_f32_e32 v136, v66, v67
	v_pk_add_f32 v[158:159], v[238:239], v[242:243]
	v_pk_fma_f32 v[84:85], v[90:91], s[10:11], v[88:89] op_sel_hi:[1,0,1]
	v_add_f32_e32 v88, v78, v79
	v_add_f32_e32 v89, v72, v73
	v_add_f32_e32 v131, v134, v131
	v_add_f32_e32 v134, v136, v135
	v_pk_add_f32 v[158:159], v[158:159], v[244:245]
	v_add_f32_e32 v88, v89, v88
	v_add_f32_e32 v89, v84, v85
	v_add_f32_e32 v137, v80, v81
	v_add_f32_e32 v134, 0, v134
	v_pk_mul_f32 v[142:143], v[142:143], s[8:9] op_sel_hi:[1,0]
	v_pk_add_f32 v[76:77], v[158:159], v[152:153]
	v_add_f32_e32 v90, v92, v93
	v_add_f32_e32 v91, v82, v83
	v_add_f32_e32 v89, v137, v89
	v_add_f32_e32 v88, v134, v88
	v_pk_mul_f32 v[144:145], v[144:145], s[8:9] op_sel_hi:[1,0]
	v_pk_add_f32 v[70:71], v[70:71], v[156:157]
	v_pk_fma_f32 v[76:77], v[76:77], s[10:11], v[142:143] op_sel_hi:[1,0,1]
	v_add_f32_e32 v90, v91, v90
	v_add_f32_e32 v91, v64, v65
	v_add_f32_e32 v142, v86, v87
	v_add_f32_e32 v88, v88, v89
	v_pk_fma_f32 v[70:71], v[70:71], s[10:11], v[144:145] op_sel_hi:[1,0,1]
	v_add_f32_e32 v94, v132, v133
	v_add_f32_e32 v95, v74, v75
	v_add_f32_e32 v91, v142, v91
	v_add_f32_e32 v88, v88, v90
	v_add_f32_e32 v94, v95, v94
	v_add_f32_e32 v95, v70, v71
	v_add_f32_e32 v143, v76, v77
	v_add_f32_e32 v88, v88, v91
	v_add_f32_e32 v95, v143, v95
	v_add_f32_e32 v88, v88, v94
	v_add_f32_e32 v88, v88, v95
	v_add_f32_e32 v88, v88, v131
	s_nop 1
	v_add_f32_dpp v88, v88, v88 quad_perm:[1,0,3,2] row_mask:0xf bank_mask:0xf bound_ctrl:1
	s_nop 1
	v_add_f32_dpp v88, v88, v88 quad_perm:[2,3,0,1] row_mask:0xf bank_mask:0xf bound_ctrl:1
	s_nop 1
	v_add_f32_dpp v88, v88, v88 row_half_mirror row_mask:0xf bank_mask:0xf bound_ctrl:1
	s_nop 1
	v_add_f32_dpp v88, v88, v88 row_mirror row_mask:0xf bank_mask:0xf bound_ctrl:1
	v_mov_b32_e32 v89, v88
	s_nop 1
	v_permlane16_swap_b32_e32 v88, v89
	v_add_f32_e32 v88, v88, v89
	v_mov_b32_e32 v89, v88
	s_nop 1
	v_permlane32_swap_b32_e32 v88, v89
	v_add_f32_e32 v88, v88, v89
	v_fmac_f32_e32 v69, 0xba000000, v88
	v_fmac_f32_e32 v67, 0xba000000, v88
	v_fmac_f32_e32 v79, 0xba000000, v88
	v_fmac_f32_e32 v73, 0xba000000, v88
	v_fmamk_f32 v68, v88, 0xba000000, v68
	v_fmamk_f32 v66, v88, 0xba000000, v66
	v_fmamk_f32 v78, v88, 0xba000000, v78
	v_fmamk_f32 v72, v88, 0xba000000, v72
	v_fmamk_f32 v84, v88, 0xba000000, v84
	v_fmac_f32_e32 v85, 0xba000000, v88
	v_fmamk_f32 v80, v88, 0xba000000, v80
	v_fmac_f32_e32 v81, 0xba000000, v88
	v_fmamk_f32 v92, v88, 0xba000000, v92
	v_fmac_f32_e32 v93, 0xba000000, v88
	v_fmamk_f32 v82, v88, 0xba000000, v82
	v_fmac_f32_e32 v83, 0xba000000, v88
	v_fmamk_f32 v64, v88, 0xba000000, v64
	v_fmac_f32_e32 v65, 0xba000000, v88
	v_fmamk_f32 v86, v88, 0xba000000, v86
	v_fmac_f32_e32 v87, 0xba000000, v88
	v_fmamk_f32 v132, v88, 0xba000000, v132
	v_fmac_f32_e32 v133, 0xba000000, v88
	v_fmamk_f32 v74, v88, 0xba000000, v74
	v_fmac_f32_e32 v75, 0xba000000, v88
	v_fmamk_f32 v70, v88, 0xba000000, v70
	v_fmac_f32_e32 v71, 0xba000000, v88
	v_fmamk_f32 v76, v88, 0xba000000, v76
	v_fmac_f32_e32 v77, 0xba000000, v88
	v_fmamk_f32 v140, v88, 0xba000000, v140
	v_fmac_f32_e32 v141, 0xba000000, v88
	v_fmamk_f32 v138, v88, 0xba000000, v138
	v_fmac_f32_e32 v139, 0xba000000, v88
	v_mul_f32_e32 v88, v67, v67
	v_mul_f32_e32 v89, v69, v69
	v_mul_f32_e32 v90, v73, v73
	v_mul_f32_e32 v91, v79, v79
	v_mul_f32_e32 v94, v81, v81
	v_mul_f32_e32 v95, v85, v85
	v_fmac_f32_e32 v88, v66, v66
	v_fmac_f32_e32 v89, v68, v68
	v_fmac_f32_e32 v90, v72, v72
	v_fmac_f32_e32 v91, v78, v78
	v_mul_f32_e32 v131, v83, v83
	v_mul_f32_e32 v134, v93, v93
	v_fmac_f32_e32 v94, v80, v80
	v_fmac_f32_e32 v95, v84, v84
	v_add_f32_e32 v88, v88, v89
	v_add_f32_e32 v89, v90, v91
	v_mul_f32_e32 v135, v87, v87
	v_mul_f32_e32 v136, v65, v65
	v_fmac_f32_e32 v131, v82, v82
	v_fmac_f32_e32 v134, v92, v92
	v_add_f32_e32 v90, v94, v95
	v_add_f32_e32 v88, v88, v89
	v_mul_f32_e32 v137, v75, v75
	v_mul_f32_e32 v142, v133, v133
	v_fmac_f32_e32 v135, v86, v86
	v_fmac_f32_e32 v136, v64, v64
	v_add_f32_e32 v91, v131, v134
	v_add_f32_e32 v88, v88, v90
	v_mul_f32_e32 v143, v77, v77
	v_mul_f32_e32 v144, v71, v71
	v_fmac_f32_e32 v137, v74, v74
	v_fmac_f32_e32 v142, v132, v132
	v_add_f32_e32 v94, v135, v136
	v_add_f32_e32 v88, v88, v91
	v_mul_f32_e32 v145, v139, v139
	v_mul_f32_e32 v146, v141, v141
	v_fmac_f32_e32 v143, v76, v76
	v_fmac_f32_e32 v144, v70, v70
	v_add_f32_e32 v95, v137, v142
	v_add_f32_e32 v88, v88, v94
	v_fmac_f32_e32 v145, v138, v138
	v_fmac_f32_e32 v146, v140, v140
	v_add_f32_e32 v131, v143, v144
	v_add_f32_e32 v88, v88, v95
	v_add_f32_e32 v134, v145, v146
	v_add_f32_e32 v88, v88, v131
	v_add_f32_e32 v88, v88, v134
	s_nop 1
	v_add_f32_dpp v88, v88, v88 quad_perm:[1,0,3,2] row_mask:0xf bank_mask:0xf bound_ctrl:1
	s_nop 1
	v_add_f32_dpp v88, v88, v88 quad_perm:[2,3,0,1] row_mask:0xf bank_mask:0xf bound_ctrl:1
	s_nop 1
	v_add_f32_dpp v88, v88, v88 row_half_mirror row_mask:0xf bank_mask:0xf bound_ctrl:1
	s_nop 1
	v_add_f32_dpp v88, v88, v88 row_mirror row_mask:0xf bank_mask:0xf bound_ctrl:1
	v_mov_b32_e32 v89, v88
	s_nop 1
	v_permlane16_swap_b32_e32 v88, v89
	v_add_f32_e32 v88, v88, v89
	v_mov_b32_e32 v89, v88
	s_nop 1
	v_permlane32_swap_b32_e32 v88, v89
	v_add_f32_e32 v88, v88, v89
	v_fmamk_f32 v88, v88, 0x3a000000, v127
	v_mul_f32_e32 v89, 0x4f800000, v88
	v_cmp_gt_f32_e32 vcc, s20, v88
	s_nop 1
	v_cndmask_b32_e32 v88, v88, v89, vcc
	v_sqrt_f32_e32 v89, v88
	s_nop 0
	v_add_u32_e32 v90, -1, v89
	v_add_u32_e32 v91, 1, v89
	v_fma_f32 v94, -v90, v89, v88
	v_fma_f32 v95, -v91, v89, v88
	v_cmp_ge_f32_e64 s[2:3], 0, v94
	s_nop 1
	v_cndmask_b32_e64 v89, v89, v90, s[2:3]
	v_cmp_lt_f32_e64 s[2:3], 0, v95
	s_nop 1
	v_cndmask_b32_e64 v89, v89, v91, s[2:3]
	v_mul_f32_e32 v90, 0x37800000, v89
	v_cndmask_b32_e32 v89, v89, v90, vcc
	v_cmp_class_f32_e32 vcc, v88, v128
	s_nop 1
	v_cndmask_b32_e32 v88, v89, v88, vcc
	v_div_scale_f32 v89, s[2:3], v88, v88, 1.0
	v_rcp_f32_e32 v91, v89
	v_div_scale_f32 v90, vcc, 1.0, v88, 1.0
	v_fma_f32 v94, -v89, v91, 1.0
	v_fmac_f32_e32 v91, v94, v91
	v_mul_f32_e32 v94, v90, v91
	v_fma_f32 v95, -v89, v94, v90
	v_fmac_f32_e32 v94, v95, v91
	v_fma_f32 v89, -v89, v94, v90
	v_div_fmas_f32 v89, v89, v91, v94
	v_div_fixup_f32 v88, v89, v88, 1.0
	v_pk_mul_f32 v[66:67], v[88:89], v[66:67] op_sel_hi:[0,1]
	v_pk_mul_f32 v[68:69], v[88:89], v[68:69] op_sel_hi:[0,1]
	v_pk_mul_f32 v[72:73], v[88:89], v[72:73] op_sel_hi:[0,1]
	v_pk_mul_f32 v[78:79], v[88:89], v[78:79] op_sel_hi:[0,1]
	v_pk_mul_f32 v[80:81], v[88:89], v[80:81] op_sel_hi:[0,1]
	v_pk_mul_f32 v[84:85], v[88:89], v[84:85] op_sel_hi:[0,1]
	v_pk_mul_f32 v[82:83], v[88:89], v[82:83] op_sel_hi:[0,1]
	v_pk_mul_f32 v[90:91], v[88:89], v[92:93] op_sel_hi:[0,1]
	v_pk_mul_f32 v[86:87], v[88:89], v[86:87] op_sel_hi:[0,1]
	v_pk_mul_f32 v[64:65], v[88:89], v[64:65] op_sel_hi:[0,1]
	v_pk_mul_f32 v[74:75], v[88:89], v[74:75] op_sel_hi:[0,1]
	v_pk_mul_f32 v[92:93], v[88:89], v[132:133] op_sel_hi:[0,1]
	v_pk_mul_f32 v[76:77], v[88:89], v[76:77] op_sel_hi:[0,1]
	v_pk_mul_f32 v[70:71], v[88:89], v[70:71] op_sel_hi:[0,1]
	v_pk_mul_f32 v[94:95], v[88:89], v[140:141] op_sel_hi:[0,1]
	v_pk_mul_f32 v[88:89], v[88:89], v[138:139] op_sel_hi:[0,1]
	s_waitcnt lgkmcnt(13)
	v_pk_fma_f32 v[18:19], v[68:69], v[18:19], v[50:51]
	v_pk_fma_f32 v[16:17], v[66:67], v[16:17], v[48:49]
	s_mov_b64 vcc, s[0:1]
	s_waitcnt lgkmcnt(12)
	v_pk_fma_f32 v[2:3], v[78:79], v[2:3], v[34:35]
	v_pk_fma_f32 v[0:1], v[72:73], v[0:1], v[32:33]
	s_waitcnt lgkmcnt(9)
	v_pk_fma_f32 v[22:23], v[84:85], v[22:23], v[54:55]
	v_pk_fma_f32 v[20:21], v[80:81], v[20:21], v[52:53]
	s_waitcnt lgkmcnt(8)
	v_pk_fma_f32 v[6:7], v[90:91], v[6:7], v[38:39]
	v_pk_fma_f32 v[4:5], v[82:83], v[4:5], v[36:37]
	s_waitcnt lgkmcnt(5)
	v_pk_fma_f32 v[26:27], v[64:65], v[26:27], v[58:59]
	v_pk_fma_f32 v[24:25], v[86:87], v[24:25], v[56:57]
	s_waitcnt lgkmcnt(4)
	v_pk_fma_f32 v[10:11], v[92:93], v[10:11], v[42:43]
	v_pk_fma_f32 v[8:9], v[74:75], v[8:9], v[40:41]
	s_waitcnt lgkmcnt(1)
	v_pk_fma_f32 v[30:31], v[70:71], v[30:31], v[62:63]
	v_pk_fma_f32 v[28:29], v[76:77], v[28:29], v[60:61]
	s_waitcnt lgkmcnt(0)
	v_pk_fma_f32 v[12:13], v[88:89], v[12:13], v[44:45]
	v_pk_fma_f32 v[14:15], v[94:95], v[14:15], v[46:47]
	global_store_dwordx4 v[116:117], v[16:19], off sc0 sc1
	global_store_dwordx4 v[116:117], v[0:3], off offset:1024 sc0 sc1
	global_store_dwordx4 v[116:117], v[20:23], off offset:2048 sc0 sc1
	global_store_dwordx4 v[116:117], v[4:7], off offset:3072 sc0 sc1
	global_store_dwordx4 v[118:119], v[24:27], off sc0 sc1
	global_store_dwordx4 v[120:121], v[8:11], off sc0 sc1
	global_store_dwordx4 v[122:123], v[28:31], off sc0 sc1
	global_store_dwordx4 v[124:125], v[12:15], off sc0 sc1
	s_cbranch_vccnz .LBB0_1205
